# arrive without waiting for store completion; upart reads validated by NaN tags with retry; prep writes NaN sentinel
# baseline (speedup 1.0000x reference)
.LBB0_18:
	s_load_dwordx4 s[4:7], s[0:1], 0x0
	v_lshl_add_u32 v4, s2, 8, v0
	v_lshrrev_b32_e32 v1, 1, v0
	v_and_b32_e32 v2, 31, v0
	s_movk_i32 s2, 0x60
	v_lshrrev_b32_e32 v0, 2, v0
	v_and_or_b32 v1, v1, s2, v2
	v_ashrrev_i32_e32 v2, 5, v4
	v_and_b32_e32 v0, 8, v0
	v_and_or_b32 v0, v2, -16, v0
	v_and_b32_e32 v2, 0x100, v4
	s_waitcnt lgkmcnt(0)
	v_mov_b32_e32 v3, s7
	v_mov_b32_e32 v5, s5
	v_cmp_eq_u32_e32 vcc, 0, v2
	v_mov_b32_e32 v2, s6
	v_lshlrev_b32_e32 v6, 2, v1
	v_cndmask_b32_e32 v3, v3, v5, vcc
	v_mov_b32_e32 v5, s4
	v_cndmask_b32_e32 v2, v2, v5, vcc
	v_mov_b32_e32 v7, 0
	v_ashrrev_i32_e32 v1, 31, v0
	v_or_b32_e32 v10, 2, v0
	v_lshl_add_u64 v[2:3], v[2:3], 0, v[6:7]
	v_lshlrev_b64 v[6:7], 9, v[0:1]
	v_or_b32_e32 v8, 1, v0
	v_ashrrev_i32_e32 v11, 31, v10
	v_or_b32_e32 v12, 3, v0
	v_or_b32_e32 v14, 4, v0
	v_or_b32_e32 v16, 5, v0
	v_or_b32_e32 v18, 6, v0
	v_or_b32_e32 v0, 7, v0
	v_ashrrev_i32_e32 v9, 31, v8
	v_lshlrev_b64 v[10:11], 9, v[10:11]
	v_ashrrev_i32_e32 v13, 31, v12
	v_ashrrev_i32_e32 v15, 31, v14
	v_ashrrev_i32_e32 v17, 31, v16
	v_ashrrev_i32_e32 v19, 31, v18
	v_ashrrev_i32_e32 v1, 31, v0
	v_lshlrev_b64 v[8:9], 9, v[8:9]
	v_lshl_add_u64 v[10:11], v[2:3], 0, v[10:11]
	v_lshlrev_b64 v[12:13], 9, v[12:13]
	v_lshlrev_b64 v[14:15], 9, v[14:15]
	v_lshlrev_b64 v[16:17], 9, v[16:17]
	v_lshlrev_b64 v[18:19], 9, v[18:19]
	v_lshlrev_b64 v[0:1], 9, v[0:1]
	v_lshl_add_u64 v[6:7], v[2:3], 0, v[6:7]
	v_lshl_add_u64 v[8:9], v[2:3], 0, v[8:9]
	v_lshl_add_u64 v[12:13], v[2:3], 0, v[12:13]
	v_lshl_add_u64 v[14:15], v[2:3], 0, v[14:15]
	v_lshl_add_u64 v[16:17], v[2:3], 0, v[16:17]
	v_lshl_add_u64 v[18:19], v[2:3], 0, v[18:19]
	v_lshl_add_u64 v[0:1], v[2:3], 0, v[0:1]
	global_load_dword v20, v[10:11], off
	global_load_dword v21, v[12:13], off
	global_load_dword v2, v[14:15], off
	global_load_dword v3, v[18:19], off
	global_load_dword v22, v[0:1], off
	global_load_dword v23, v[16:17], off
	global_load_dword v24, v[6:7], off
	global_load_dword v25, v[8:9], off
	s_load_dwordx4 s[8:11], s[0:1], 0x40
	v_ashrrev_i32_e32 v5, 31, v4
	s_waitcnt lgkmcnt(0)
	v_lshl_add_u64 v[26:27], v[4:5], 2, s[10:11]
	v_lshl_add_u64 v[4:5], v[4:5], 4, s[8:9]
	s_waitcnt vmcnt(6)
	v_cvt_pk_f16_f32 v1, v20, v21
	s_waitcnt vmcnt(3)
	v_cvt_pk_f16_f32 v3, v3, v22
	s_waitcnt vmcnt(2)
	v_cvt_pk_f16_f32 v2, v2, v23
	s_waitcnt vmcnt(0)
	v_cvt_pk_f16_f32 v0, v24, v25
	global_store_dwordx4 v[4:5], v[0:3], off
	v_mov_b32_e32 v28, 0x7fc00000
	v_add_co_u32_e32 v26, vcc, 0x1e000, v26
	s_nop 1
	v_addc_co_u32_e32 v27, vcc, 0, v27, vcc
	global_store_dword v[26:27], v28, off
	s_endpgm

.LBB1_5:
	s_ashr_i32 s43, s2, 5
	s_and_b64 s[4:5], s[4:5], exec
	s_cselect_b32 s42, 4, 3
	s_lshl_b32 s4, s45, 5
	s_mul_i32 s33, s43, 0xfa0
	v_and_b32_e32 v212, 63, v0
	v_lshrrev_b32_e32 v68, 6, v0
	s_add_i32 s33, s33, s4
	s_add_i32 s44, s43, s2
	s_and_b32 s24, s44, 7
	v_lshlrev_b32_e32 v213, 4, v212
	v_or_b32_e32 v1, s33, v68
	v_bfe_u32 v224, v0, 6, 2
	v_lshrrev_b32_e32 v225, 8, v0
	v_lshl_or_b32 v197, v1, 13, v213
	v_lshlrev_b32_e32 v1, 12, v225
	v_lshlrev_b32_e32 v2, 6, v224
	s_lshl_b32 s4, s24, 17
	v_or3_b32 v1, v2, v1, v212
	s_waitcnt lgkmcnt(0)
	s_add_u32 s4, s40, s4
	v_lshlrev_b32_e32 v66, 4, v1
	s_addc_u32 s5, s41, 0
	v_mov_b32_e32 v67, 0
	v_lshl_add_u64 v[2:3], s[4:5], 0, v[66:67]
	s_movk_i32 s6, 0x2000
	v_add_co_u32_e32 v4, vcc, s6, v2
	s_and_b32 s21, s21, 0xffff
	s_nop 0
	v_addc_co_u32_e32 v5, vcc, 0, v3, vcc
	global_load_dwordx4 v[118:121], v66, s[4:5]
	global_load_dwordx4 v[114:117], v[4:5], off offset:-4096
	s_movk_i32 s4, 0x4000
	v_add_co_u32_e32 v6, vcc, s4, v2
	s_movk_i32 s4, 0x6000
	s_nop 0
	v_addc_co_u32_e32 v7, vcc, 0, v3, vcc
	global_load_dwordx4 v[90:93], v[4:5], off
	global_load_dwordx4 v[98:101], v[6:7], off offset:-4096
	v_add_co_u32_e32 v4, vcc, s4, v2
	s_movk_i32 s4, 0x7000
	s_nop 0
	v_addc_co_u32_e32 v5, vcc, 0, v3, vcc
	v_add_co_u32_e32 v2, vcc, s4, v2
	s_lshl_b32 s24, s24, 10
	s_mov_b32 s7, 0x20000
	v_addc_co_u32_e32 v3, vcc, 0, v3, vcc
	s_mov_b32 s6, 0xfa00000
	s_mov_b32 s4, s20
	s_mov_b32 s5, s21
	s_or_b32 s25, s24, 0x40000
	v_or_b32_e32 v198, 0x10000, v197
	v_or_b32_e32 v199, 0x20000, v197
	v_or_b32_e32 v200, 0x30000, v197
	global_load_dwordx4 v[102:105], v[6:7], off
	global_load_dwordx4 v[94:97], v[4:5], off offset:-4096
	global_load_dwordx4 v[82:85], v[4:5], off
	global_load_dwordx4 v[86:89], v[2:3], off
	buffer_load_dwordx4 v[62:65], v197, s[4:7], s24 offen sc0 nt sc1
	buffer_load_dwordx4 v[46:49], v197, s[4:7], s25 offen sc0 nt sc1
	buffer_load_dwordx4 v[58:61], v198, s[4:7], s24 offen sc0 nt sc1
	buffer_load_dwordx4 v[42:45], v198, s[4:7], s25 offen sc0 nt sc1
	buffer_load_dwordx4 v[54:57], v199, s[4:7], s24 offen sc0 nt sc1
	buffer_load_dwordx4 v[38:41], v199, s[4:7], s25 offen sc0 nt sc1
	buffer_load_dwordx4 v[50:53], v200, s[4:7], s24 offen sc0 nt sc1
	buffer_load_dwordx4 v[34:37], v200, s[4:7], s25 offen sc0 nt sc1
	s_or_b32 s25, s24, 0x80000
	s_or_b32 s3, s24, s3
	buffer_load_dwordx4 v[30:33], v197, s[4:7], s25 offen sc0 nt sc1
	buffer_load_dwordx4 v[14:17], v197, s[4:7], s3 offen sc0 nt sc1
	buffer_load_dwordx4 v[26:29], v198, s[4:7], s25 offen sc0 nt sc1
	buffer_load_dwordx4 v[10:13], v198, s[4:7], s3 offen sc0 nt sc1
	buffer_load_dwordx4 v[22:25], v199, s[4:7], s25 offen sc0 nt sc1
	buffer_load_dwordx4 v[6:9], v199, s[4:7], s3 offen sc0 nt sc1
	buffer_load_dwordx4 v[18:21], v200, s[4:7], s25 offen sc0 nt sc1
	buffer_load_dwordx4 v[2:5], v200, s[4:7], s3 offen sc0 nt sc1
	s_lshl_b32 s3, s44, 10
	s_addk_i32 s3, 0x400
	s_and_b32 s3, s3, 0x1c00
	s_or_b32 s24, s3, 0x40000
	buffer_load_dwordx4 v[142:145], v197, s[4:7], s3 offen sc0 nt sc1
	buffer_load_dwordx4 v[126:129], v197, s[4:7], s24 offen sc0 nt sc1
	buffer_load_dwordx4 v[138:141], v198, s[4:7], s3 offen sc0 nt sc1
	buffer_load_dwordx4 v[122:125], v198, s[4:7], s24 offen sc0 nt sc1
	buffer_load_dwordx4 v[134:137], v199, s[4:7], s3 offen sc0 nt sc1
	buffer_load_dwordx4 v[110:113], v199, s[4:7], s24 offen sc0 nt sc1
	buffer_load_dwordx4 v[130:133], v200, s[4:7], s3 offen sc0 nt sc1
	buffer_load_dwordx4 v[106:109], v200, s[4:7], s24 offen sc0 nt sc1
	s_load_dwordx2 s[24:25], s[0:1], 0x70
	s_load_dwordx2 s[34:35], s[0:1], 0x60
	s_load_dwordx2 s[36:37], s[0:1], 0x40
	s_load_dwordx4 s[68:71], s[0:1], 0x18
	s_mov_b32 s73, 0
	s_mov_b32 s47, 0
	s_lshl_b32 s4, s45, 2
	s_and_b32 s4, s4, 0x1ffc
	s_mulk_i32 s4, 0x147b
	s_lshr_b32 s38, s4, 17
	s_add_i32 s50, s38, 1
	s_cmpk_lt_u32 s45, 0x77
	s_mul_i32 s3, s43, 20
	s_cselect_b32 s4, s50, 19
	s_add_i32 s4, s4, s3
	s_ashr_i32 s5, s4, 31
	s_lshl_b64 s[4:5], s[4:5], 2
	s_add_u32 s4, s22, s4
	s_addc_u32 s5, s23, s5
	s_add_i32 s38, s3, s38
	s_ashr_i32 s39, s38, 31
	s_lshl_b64 s[38:39], s[38:39], 2
	s_add_u32 s38, s22, s38
	s_addc_u32 s39, s23, s39
	s_load_dword s48, s[38:39], 0x0
	s_load_dword s49, s[4:5], 0x0
	s_mulk_i32 s50, 0xc8
	s_mov_b32 s38, 24
	s_mov_b32 s51, s45
	s_mov_b32 s52, s50
	s_waitcnt lgkmcnt(0)
	s_mov_b32 s53, s48
	s_mov_b32 s54, s49
	v_mov_b32_e32 v1, v68
	s_mov_b32 s55, s42
	s_mov_b32 s56, 16
	s_mov_b32 s39, s38
	v_mov_b32_e32 v69, v67
	v_mov_b32_e32 v70, v67

.LBB1_18:
	s_or_b64 exec, exec, s[0:1]
	v_cmp_eq_u32_e32 vcc, 0, v0
	s_waitcnt lgkmcnt(0)
	s_and_saveexec_b64 s[0:1], vcc
	s_cbranch_execz .LBB1_21
	s_mov_b64 s[20:21], exec
	v_mbcnt_lo_u32_b32 v66, s20, 0
	v_mbcnt_hi_u32_b32 v66, s21, v66
	v_cmp_eq_u32_e32 vcc, 0, v66
	s_and_b64 s[38:39], exec, vcc
	s_mov_b64 exec, s[38:39]
	s_cbranch_execz .LBB1_21
	s_lshl_b32 s2, s2, 8
	s_and_b32 s2, s2, 0x700
	s_bcnt1_i32_b64 s20, s[20:21]
	v_mov_b32_e32 v66, s2
	v_mov_b32_e32 v67, s20
	global_atomic_add v66, v67, s[6:7]

.Lsu_check:
	v_cmp_u_f32_e32 vcc, v215, v215
	s_cmp_lg_u64 vcc, 0
	s_cbranch_scc0 .Lsu_ok
	s_add_i32 s73, s73, 1
	s_cmp_gt_u32 s73, 0x10000
	s_cbranch_scc1 .Lsu_ok
	s_sleep 2
	v_and_b32_e32 v247, 0x7f, v0
	v_lshrrev_b32_e32 v248, 7, v0
	s_lshl_b32 s72, s43, 13
	v_lshl_or_b32 v247, v248, 11, v247
	v_or_b32_e32 v247, s72, v247
	v_lshlrev_b32_e32 v247, 2, v247
	global_load_dword v248, v247, s[68:69] sc1
	global_load_dword v249, v247, s[68:69] offset:512 sc1
	global_load_dword v250, v247, s[68:69] offset:1024 sc1
	global_load_dword v251, v247, s[68:69] offset:1536 sc1
	global_load_dword v252, v247, s[68:69] offset:2048 sc1
	global_load_dword v253, v247, s[68:69] offset:2560 sc1
	global_load_dword v254, v247, s[68:69] offset:3072 sc1
	global_load_dword v255, v247, s[68:69] offset:3584 sc1
	s_waitcnt vmcnt(0)
	v_add_f32_e32 v215, 0, v248
	v_add_f32_e32 v215, v215, v249
	v_add_f32_e32 v215, v215, v250
	v_add_f32_e32 v215, v215, v251
	v_add_f32_e32 v215, v215, v252
	v_add_f32_e32 v215, v215, v253
	v_add_f32_e32 v215, v215, v254
	v_add_f32_e32 v215, v215, v255
	v_add_u32_e32 v247, 0x1000, v247
	global_load_dword v248, v247, s[68:69] sc1
	global_load_dword v249, v247, s[68:69] offset:512 sc1
	global_load_dword v250, v247, s[68:69] offset:1024 sc1
	global_load_dword v251, v247, s[68:69] offset:1536 sc1
	global_load_dword v252, v247, s[68:69] offset:2048 sc1
	global_load_dword v253, v247, s[68:69] offset:2560 sc1
	global_load_dword v254, v247, s[68:69] offset:3072 sc1
	global_load_dword v255, v247, s[68:69] offset:3584 sc1
	s_waitcnt vmcnt(0)
	v_add_f32_e32 v215, v215, v248
	v_add_f32_e32 v215, v215, v249
	v_add_f32_e32 v215, v215, v250
	v_add_f32_e32 v215, v215, v251
	v_add_f32_e32 v215, v215, v252
	v_add_f32_e32 v215, v215, v253
	v_add_f32_e32 v215, v215, v254
	v_add_f32_e32 v215, v215, v255
	s_branch .Lsu_check
.Lsu_ok:
	v_add_u32_e32 v213, 0x17280, v210
	ds_write2st64_b32 v210, v239, v240 offset1:8
	ds_write2st64_b32 v210, v242, v241 offset0:16 offset1:24
	ds_write_b32 v210, v243 offset:8192
	ds_write_b32 v213, v215
	v_and_or_b32 v215, v0, s4, v238
	v_mov_b32_e32 v238, 0x17a80
	s_movk_i32 s4, 0x80
	v_lshl_add_u32 v215, v215, 2, v238
	v_cmp_gt_u32_e64 s[4:5], s4, v0
	ds_write_b32 v215, v246
	s_waitcnt lgkmcnt(0)
	s_barrier
	s_and_saveexec_b64 s[6:7], s[4:5]
	s_cbranch_execz .LBB1_42
	v_add_u32_e32 v215, 0x17280, v226
	ds_read2st64_b32 v[238:239], v213 offset0:2 offset1:4
	ds_read_b32 v215, v215
	ds_read2st64_b32 v[240:241], v213 offset0:6 offset1:8
	ds_read2st64_b32 v[242:243], v213 offset0:10 offset1:12
	ds_read_b32 v213, v213 offset:3584
	s_waitcnt lgkmcnt(3)
	v_add_f32_e32 v215, v215, v238
	v_add_f32_e32 v215, v215, v239
	s_waitcnt lgkmcnt(2)
	v_add_f32_e32 v215, v215, v240
	v_div_scale_f32 v238, s[8:9], v245, v245, v215
	v_rcp_f32_e32 v239, v238
	s_waitcnt lgkmcnt(1)
	v_add_f32_e32 v240, v241, v242
	v_add_f32_e32 v240, v240, v243
	s_waitcnt lgkmcnt(0)
	v_add_f32_e32 v213, v240, v213
	v_fma_f32 v240, -v238, v239, 1.0
	v_fmac_f32_e32 v239, v240, v239
	v_div_scale_f32 v240, vcc, v215, v245, v215
	v_mul_f32_e32 v241, v240, v239
	v_fma_f32 v242, -v238, v241, v240
	v_fmac_f32_e32 v241, v242, v239
	v_fma_f32 v238, -v238, v241, v240
	v_div_fmas_f32 v238, v238, v239, v241
	v_div_fixup_f32 v215, v238, v245, v215
	v_add_f32_e32 v215, v237, v215
	v_add_f32_e32 v213, v215, v213
	v_max_f32_e32 v213, 0, v213
	v_add_u32_e32 v215, 0x1b280, v226
	ds_write_b32 v215, v213

	.amdhsa_kernel _Z12fused_kernelPKfPKiPKDF16_PfPjS0_S0_S0_S0_S0_S0_S0_S0_S0_S0_S0_S5_
		.amdhsa_group_segment_fixed_size 163840
		.amdhsa_private_segment_fixed_size 0
		.amdhsa_kernarg_size 136
		.amdhsa_user_sgpr_count 2
		.amdhsa_user_sgpr_dispatch_ptr 0
		.amdhsa_user_sgpr_queue_ptr 0
		.amdhsa_user_sgpr_kernarg_segment_ptr 1
		.amdhsa_user_sgpr_dispatch_id 0
		.amdhsa_user_sgpr_kernarg_preload_length 0
		.amdhsa_user_sgpr_kernarg_preload_offset 0
		.amdhsa_user_sgpr_private_segment_size 0
		.amdhsa_uses_dynamic_stack 0
		.amdhsa_enable_private_segment 0
		.amdhsa_system_sgpr_workgroup_id_x 1
		.amdhsa_system_sgpr_workgroup_id_y 0
		.amdhsa_system_sgpr_workgroup_id_z 0
		.amdhsa_system_sgpr_workgroup_info 0
		.amdhsa_system_vgpr_workitem_id 0
		.amdhsa_next_free_vgpr 256
		.amdhsa_next_free_sgpr 96
		.amdhsa_accum_offset 256
		.amdhsa_reserve_vcc 1
		.amdhsa_float_round_mode_32 0
		.amdhsa_float_round_mode_16_64 0
		.amdhsa_float_denorm_mode_32 3
		.amdhsa_float_denorm_mode_16_64 3
		.amdhsa_dx10_clamp 1
		.amdhsa_ieee_mode 1
		.amdhsa_fp16_overflow 0
		.amdhsa_tg_split 0
		.amdhsa_exception_fp_ieee_invalid_op 0
		.amdhsa_exception_fp_denorm_src 0
		.amdhsa_exception_fp_ieee_div_zero 0
		.amdhsa_exception_fp_ieee_overflow 0
		.amdhsa_exception_fp_ieee_underflow 0
		.amdhsa_exception_fp_ieee_inexact 0
		.amdhsa_exception_int_div_zero 0
	.end_amdhsa_kernel

amdhsa.kernels:
  - .agpr_count:     0
    .args:
      - .actual_access:  read_only
        .address_space:  global
        .offset:         0
        .size:           8
        .value_kind:     global_buffer
      - .actual_access:  read_only
        .address_space:  global
        .offset:         8
        .size:           8
        .value_kind:     global_buffer
      - .actual_access:  read_only
        .address_space:  global
        .offset:         16
        .size:           8
        .value_kind:     global_buffer
      - .actual_access:  read_only
        .address_space:  global
        .offset:         24
        .size:           8
        .value_kind:     global_buffer
      - .actual_access:  read_only
        .address_space:  global
        .offset:         32
        .size:           8
        .value_kind:     global_buffer
      - .actual_access:  read_only
        .address_space:  global
        .offset:         40
        .size:           8
        .value_kind:     global_buffer
      - .actual_access:  read_only
        .address_space:  global
        .offset:         48
        .size:           8
        .value_kind:     global_buffer
      - .actual_access:  read_only
        .address_space:  global
        .offset:         56
        .size:           8
        .value_kind:     global_buffer
      - .actual_access:  write_only
        .address_space:  global
        .offset:         64
        .size:           8
        .value_kind:     global_buffer
      - .actual_access:  write_only
        .address_space:  global
        .offset:         72
        .size:           8
        .value_kind:     global_buffer
      - .actual_access:  write_only
        .address_space:  global
        .offset:         80
        .size:           8
        .value_kind:     global_buffer
      - .actual_access:  write_only
        .address_space:  global
        .offset:         88
        .size:           8
        .value_kind:     global_buffer
    .group_segment_fixed_size: 512
    .kernarg_segment_align: 8
    .kernarg_segment_size: 96
    .language:       OpenCL C
    .language_version:
      - 2
      - 0
    .max_flat_workgroup_size: 256
    .name:           _Z11prep_kernelPKfS0_S0_S0_S0_S0_S0_S0_PDF16_PfS2_Pj
    .private_segment_fixed_size: 0
    .sgpr_count:     18
    .sgpr_spill_count: 0
    .symbol:         _Z11prep_kernelPKfS0_S0_S0_S0_S0_S0_S0_PDF16_PfS2_Pj.kd
    .uniform_work_group_size: 1
    .uses_dynamic_stack: false
    .vgpr_count:     67
    .vgpr_spill_count: 0
    .wavefront_size: 64
  - .agpr_count:     0
    .args:
      - .actual_access:  read_only
        .address_space:  global
        .offset:         0
        .size:           8
        .value_kind:     global_buffer
      - .actual_access:  read_only
        .address_space:  global
        .offset:         8
        .size:           8
        .value_kind:     global_buffer
      - .actual_access:  read_only
        .address_space:  global
        .offset:         16
        .size:           8
        .value_kind:     global_buffer
      - .address_space:  global
        .offset:         24
        .size:           8
        .value_kind:     global_buffer
      - .address_space:  global
        .offset:         32
        .size:           8
        .value_kind:     global_buffer
      - .actual_access:  read_only
        .address_space:  global
        .offset:         40
        .size:           8
        .value_kind:     global_buffer
      - .actual_access:  read_only
        .address_space:  global
        .offset:         48
        .size:           8
        .value_kind:     global_buffer
      - .actual_access:  read_only
        .address_space:  global
        .offset:         56
        .size:           8
        .value_kind:     global_buffer
      - .actual_access:  read_only
        .address_space:  global
        .offset:         64
        .size:           8
        .value_kind:     global_buffer
      - .actual_access:  read_only
        .address_space:  global
        .offset:         72
        .size:           8
        .value_kind:     global_buffer
      - .actual_access:  read_only
        .address_space:  global
        .offset:         80
        .size:           8
        .value_kind:     global_buffer
      - .actual_access:  read_only
        .address_space:  global
        .offset:         88
        .size:           8
        .value_kind:     global_buffer
      - .actual_access:  read_only
        .address_space:  global
        .offset:         96
        .size:           8
        .value_kind:     global_buffer
      - .actual_access:  read_only
        .address_space:  global
        .offset:         104
        .size:           8
        .value_kind:     global_buffer
      - .actual_access:  read_only
        .address_space:  global
        .offset:         112
        .size:           8
        .value_kind:     global_buffer
      - .actual_access:  read_only
        .address_space:  global
        .offset:         120
        .size:           8
        .value_kind:     global_buffer
      - .actual_access:  write_only
        .address_space:  global
        .offset:         128
        .size:           8
        .value_kind:     global_buffer
    .group_segment_fixed_size: 163840
    .kernarg_segment_align: 8
    .kernarg_segment_size: 136
    .language:       OpenCL C
    .language_version:
      - 2
      - 0
    .max_flat_workgroup_size: 512
    .name:           _Z12fused_kernelPKfPKiPKDF16_PfPjS0_S0_S0_S0_S0_S0_S0_S0_S0_S0_S0_S5_
    .private_segment_fixed_size: 0
    .sgpr_count:     80
    .sgpr_spill_count: 0
    .symbol:         _Z12fused_kernelPKfPKiPKDF16_PfPjS0_S0_S0_S0_S0_S0_S0_S0_S0_S0_S0_S5_.kd
    .uniform_work_group_size: 1
    .uses_dynamic_stack: false
    .vgpr_count:     256
    .vgpr_spill_count: 0
    .wavefront_size: 64
